# baseline (speedup 1.0000x reference)
.LBB0_29:
	s_mov_b32 s29, 0
	s_lshl_b64 s[6:7], s[28:29], 2
	s_add_u32 s8, s26, s6
	s_addc_u32 s9, s27, s7
	s_add_u32 s6, s24, s6
	v_mov_b32_e32 v1, 0
	s_addc_u32 s7, s25, s7
	v_mov_b32_e32 v2, 0x3e38aa3b
	global_store_dword v1, v5, s[6:7] sc1
	global_store_dword v1, v2, s[8:9] sc1

.LBB0_32:
	s_cbranch_execz .LBB0_31
	v_or_b32_e32 v2, 1, v4
	v_lshlrev_b32_e32 v1, 2, v4
	v_or_b32_e32 v3, 2, v4
	v_lshlrev_b32_e32 v5, 2, v2
	global_store_dword v1, v4, s[22:23] sc1
	global_store_dwordx2 v5, v[2:3], s[22:23] sc1
	v_or_b32_e32 v2, 3, v4
	v_or_b32_e32 v3, 4, v4
	v_lshlrev_b32_e32 v5, 2, v2
	global_store_dwordx2 v5, v[2:3], s[22:23] sc1
	v_or_b32_e32 v2, 5, v4
	v_or_b32_e32 v3, 6, v4
	v_lshlrev_b32_e32 v5, 2, v2
	global_store_dwordx2 v5, v[2:3], s[22:23] sc1
	v_or_b32_e32 v2, 7, v4
	global_store_dword v1, v2, s[22:23] offset:28 sc1
	s_and_saveexec_b64 s[4:5], s[20:21]
	s_cbranch_execz .LBB0_35
	s_mov_b32 s29, 0
	s_lshl_b64 s[6:7], s[28:29], 2
	s_add_u32 s8, s26, s6
	s_addc_u32 s9, s27, s7
	s_add_u32 s6, s24, s6
	s_addc_u32 s7, s25, s7
	v_mov_b32_e32 v1, 0x800
	v_mov_b32_e32 v2, 0
	global_store_dword v2, v1, s[6:7] sc1
	global_store_dword v2, v2, s[8:9] sc1

.LBB0_36:
	s_load_dwordx8 s[8:15], s[0:1], 0x0
	s_lshl_b32 s3, s2, 3
	s_and_b32 s6, s3, 0x1c0
	v_lshrrev_b32_e32 v16, 6, v0
	s_lshl_b32 s3, s2, 6
	v_and_b32_e32 v17, 63, v0
	v_or_b32_e32 v0, s6, v16
	s_ashr_i32 s4, s2, 6
	s_and_b32 s7, s3, 0x1c0
	v_lshlrev_b32_e32 v0, 9, v0
	s_cmp_eq_u32 s4, 2
	v_or3_b32 v0, v17, v0, s7
	v_or_b32_e32 v19, 4, v16
	s_waitcnt lgkmcnt(0)
	s_cselect_b32 s3, s13, s15
	s_cselect_b32 s5, s12, s14
	s_cmp_eq_u32 s4, 1
	v_lshlrev_b32_e32 v18, 2, v0
	v_or_b32_e32 v0, s6, v19
	s_cselect_b32 s5, s10, s5
	s_cselect_b32 s3, s11, s3
	s_cmp_lt_u32 s2, 64
	v_lshlrev_b32_e32 v0, 9, v0
	s_cselect_b32 s3, s9, s3
	s_cselect_b32 s2, s8, s5
	v_or3_b32 v0, v17, v0, s7
	v_mov_b32_e32 v1, 0
	v_or_b32_e32 v20, 8, v16
	v_lshl_add_u64 v[2:3], v[0:1], 2, s[2:3]
	v_or_b32_e32 v0, s6, v20
	v_lshlrev_b32_e32 v0, 9, v0
	v_or3_b32 v0, v17, v0, s7
	v_or_b32_e32 v21, 12, v16
	v_lshl_add_u64 v[4:5], v[0:1], 2, s[2:3]
	v_or_b32_e32 v0, s6, v21
	v_lshlrev_b32_e32 v0, 9, v0
	v_or3_b32 v0, v17, v0, s7
	v_or_b32_e32 v22, 16, v16
	v_lshl_add_u64 v[6:7], v[0:1], 2, s[2:3]
	v_or_b32_e32 v0, s6, v22
	v_lshlrev_b32_e32 v0, 9, v0
	v_or3_b32 v0, v17, v0, s7
	v_or_b32_e32 v23, 20, v16
	v_lshl_add_u64 v[8:9], v[0:1], 2, s[2:3]
	v_or_b32_e32 v0, s6, v23
	v_lshlrev_b32_e32 v0, 9, v0
	v_or3_b32 v0, v17, v0, s7
	v_or_b32_e32 v24, 24, v16
	v_lshl_add_u64 v[10:11], v[0:1], 2, s[2:3]
	v_or_b32_e32 v0, s6, v24
	v_lshlrev_b32_e32 v0, 9, v0
	v_or3_b32 v0, v17, v0, s7
	v_or_b32_e32 v25, 28, v16
	v_lshl_add_u64 v[12:13], v[0:1], 2, s[2:3]
	v_or_b32_e32 v0, s6, v25
	v_lshlrev_b32_e32 v0, 9, v0
	v_or3_b32 v0, v17, v0, s7
	v_lshl_add_u64 v[14:15], v[0:1], 2, s[2:3]
	global_load_dword v26, v18, s[2:3]
	global_load_dword v27, v[2:3], off
	global_load_dword v28, v[4:5], off
	global_load_dword v29, v[6:7], off
	global_load_dword v30, v[8:9], off
	global_load_dword v31, v[10:11], off
	global_load_dword v32, v[12:13], off
	global_load_dword v33, v[14:15], off
	v_or_b32_e32 v18, 32, v16
	v_or_b32_e32 v0, s6, v18
	v_lshlrev_b32_e32 v0, 9, v0
	v_or3_b32 v0, v17, v0, s7
	v_or_b32_e32 v34, 36, v16
	v_lshl_add_u64 v[2:3], v[0:1], 2, s[2:3]
	v_or_b32_e32 v0, s6, v34
	v_lshlrev_b32_e32 v0, 9, v0
	v_or3_b32 v0, v17, v0, s7
	v_or_b32_e32 v35, 40, v16
	v_lshl_add_u64 v[4:5], v[0:1], 2, s[2:3]
	v_or_b32_e32 v0, s6, v35
	v_lshlrev_b32_e32 v0, 9, v0
	v_or3_b32 v0, v17, v0, s7
	v_or_b32_e32 v36, 44, v16
	v_lshl_add_u64 v[6:7], v[0:1], 2, s[2:3]
	v_or_b32_e32 v0, s6, v36
	v_lshlrev_b32_e32 v0, 9, v0
	v_or3_b32 v0, v17, v0, s7
	v_or_b32_e32 v37, 48, v16
	v_lshl_add_u64 v[8:9], v[0:1], 2, s[2:3]
	v_or_b32_e32 v0, s6, v37
	v_lshlrev_b32_e32 v0, 9, v0
	v_or3_b32 v0, v17, v0, s7
	v_or_b32_e32 v38, 52, v16
	v_lshl_add_u64 v[10:11], v[0:1], 2, s[2:3]
	v_or_b32_e32 v0, s6, v38
	v_lshlrev_b32_e32 v0, 9, v0
	v_or3_b32 v0, v17, v0, s7
	v_or_b32_e32 v39, 56, v16
	v_lshl_add_u64 v[12:13], v[0:1], 2, s[2:3]
	v_or_b32_e32 v0, s6, v39
	v_lshlrev_b32_e32 v0, 9, v0
	v_or3_b32 v0, v17, v0, s7
	v_or_b32_e32 v40, 60, v16
	v_lshl_add_u64 v[14:15], v[0:1], 2, s[2:3]
	v_or_b32_e32 v0, s6, v40
	v_lshlrev_b32_e32 v0, 9, v0
	v_or3_b32 v0, v17, v0, s7
	v_lshl_add_u64 v[0:1], v[0:1], 2, s[2:3]
	global_load_dword v41, v[2:3], off
	global_load_dword v42, v[4:5], off
	global_load_dword v43, v[6:7], off
	global_load_dword v44, v[8:9], off
	global_load_dword v45, v[10:11], off
	global_load_dword v46, v[12:13], off
	global_load_dword v47, v[14:15], off
	global_load_dword v48, v[0:1], off
	v_mul_u32_u24_e32 v0, 0x104, v16
	v_lshl_add_u32 v0, v17, 2, v0
	s_movk_i32 s2, 0x104
	s_load_dwordx2 s[0:1], s[0:1], 0x28
	s_ashr_i32 s5, s4, 31
	v_or_b32_e32 v5, s7, v16
	v_lshlrev_b32_e32 v5, 9, v5
	v_or3_b32 v5, v17, v5, s6
	v_lshlrev_b32_e32 v5, 1, v5
	s_waitcnt vmcnt(15)
	ds_write_b32 v0, v26
	s_waitcnt vmcnt(14)
	ds_write_b32 v0, v27 offset:1040
	s_waitcnt vmcnt(13)
	ds_write_b32 v0, v28 offset:2080
	s_waitcnt vmcnt(12)
	ds_write_b32 v0, v29 offset:3120
	s_waitcnt vmcnt(11)
	ds_write_b32 v0, v30 offset:4160
	s_waitcnt vmcnt(10)
	ds_write_b32 v0, v31 offset:5200
	s_waitcnt vmcnt(9)
	ds_write_b32 v0, v32 offset:6240
	s_waitcnt vmcnt(8)
	ds_write_b32 v0, v33 offset:7280
	s_waitcnt vmcnt(7)
	ds_write_b32 v0, v41 offset:8320
	s_waitcnt vmcnt(6)
	ds_write_b32 v0, v42 offset:9360
	s_waitcnt vmcnt(5)
	ds_write_b32 v0, v43 offset:10400
	s_waitcnt vmcnt(4)
	ds_write_b32 v0, v44 offset:11440
	s_waitcnt vmcnt(3)
	ds_write_b32 v0, v45 offset:12480
	s_waitcnt vmcnt(2)
	ds_write_b32 v0, v46 offset:13520
	s_waitcnt vmcnt(1)
	ds_write_b32 v0, v47 offset:14560
	s_waitcnt vmcnt(0)
	ds_write_b32 v0, v48 offset:15600
	v_lshlrev_b32_e32 v0, 2, v16
	v_mad_u32_u24 v4, v17, s2, v0
	s_waitcnt lgkmcnt(0)
	s_barrier
	ds_read2_b32 v[0:1], v4 offset1:4
	s_lshl_b64 s[2:3], s[4:5], 19
	s_add_u32 s0, s0, s2
	s_addc_u32 s1, s1, s3
	ds_read2_b32 v[2:3], v4 offset0:8 offset1:12
	s_waitcnt lgkmcnt(1)
	v_cvt_f16_f32_e32 v0, v0
	global_store_short v5, v0, s[0:1] sc1
	v_cvt_f16_f32_e32 v0, v1
	v_or_b32_e32 v1, s7, v19
	v_lshlrev_b32_e32 v1, 9, v1
	v_or3_b32 v1, v17, v1, s6
	v_lshlrev_b32_e32 v1, 1, v1
	global_store_short v1, v0, s[0:1] sc1
	s_waitcnt lgkmcnt(0)
	v_cvt_f16_f32_e32 v0, v2
	v_or_b32_e32 v1, s7, v20
	v_lshlrev_b32_e32 v1, 9, v1
	v_or3_b32 v1, v17, v1, s6
	v_lshlrev_b32_e32 v1, 1, v1
	global_store_short v1, v0, s[0:1] sc1
	ds_read2_b32 v[0:1], v4 offset0:16 offset1:20
	v_cvt_f16_f32_e32 v2, v3
	v_or_b32_e32 v3, s7, v21
	v_lshlrev_b32_e32 v3, 9, v3
	v_or3_b32 v3, v17, v3, s6
	v_lshlrev_b32_e32 v3, 1, v3
	global_store_short v3, v2, s[0:1] sc1
	s_waitcnt lgkmcnt(0)
	v_cvt_f16_f32_e32 v0, v0
	v_or_b32_e32 v2, s7, v22
	v_lshlrev_b32_e32 v2, 9, v2
	v_or3_b32 v2, v17, v2, s6
	v_lshlrev_b32_e32 v2, 1, v2
	global_store_short v2, v0, s[0:1] sc1
	v_cvt_f16_f32_e32 v2, v1
	ds_read2_b32 v[0:1], v4 offset0:24 offset1:28
	v_or_b32_e32 v3, s7, v23
	v_lshlrev_b32_e32 v3, 9, v3
	v_or3_b32 v3, v17, v3, s6
	v_lshlrev_b32_e32 v3, 1, v3
	global_store_short v3, v2, s[0:1] sc1
	s_waitcnt lgkmcnt(0)
	v_cvt_f16_f32_e32 v0, v0
	v_or_b32_e32 v2, s7, v24
	v_lshlrev_b32_e32 v2, 9, v2
	v_or3_b32 v2, v17, v2, s6
	v_lshlrev_b32_e32 v2, 1, v2
	global_store_short v2, v0, s[0:1] sc1
	v_cvt_f16_f32_e32 v2, v1
	ds_read2_b32 v[0:1], v4 offset0:32 offset1:36
	v_or_b32_e32 v3, s7, v25
	v_lshlrev_b32_e32 v3, 9, v3
	v_or3_b32 v3, v17, v3, s6
	v_lshlrev_b32_e32 v3, 1, v3
	global_store_short v3, v2, s[0:1] sc1
	s_waitcnt lgkmcnt(0)
	v_cvt_f16_f32_e32 v0, v0
	v_or_b32_e32 v2, s7, v18
	v_lshlrev_b32_e32 v2, 9, v2
	v_or3_b32 v2, v17, v2, s6
	v_lshlrev_b32_e32 v2, 1, v2
	global_store_short v2, v0, s[0:1] sc1
	v_cvt_f16_f32_e32 v2, v1
	ds_read2_b32 v[0:1], v4 offset0:40 offset1:44
	v_or_b32_e32 v3, s7, v34
	v_lshlrev_b32_e32 v3, 9, v3
	v_or3_b32 v3, v17, v3, s6
	v_lshlrev_b32_e32 v3, 1, v3
	global_store_short v3, v2, s[0:1] sc1
	s_waitcnt lgkmcnt(0)
	v_cvt_f16_f32_e32 v0, v0
	v_or_b32_e32 v2, s7, v35
	v_lshlrev_b32_e32 v2, 9, v2
	v_or3_b32 v2, v17, v2, s6
	v_lshlrev_b32_e32 v2, 1, v2
	global_store_short v2, v0, s[0:1] sc1
	v_cvt_f16_f32_e32 v2, v1
	ds_read2_b32 v[0:1], v4 offset0:48 offset1:52
	v_or_b32_e32 v3, s7, v36
	v_lshlrev_b32_e32 v3, 9, v3
	v_or3_b32 v3, v17, v3, s6
	v_lshlrev_b32_e32 v3, 1, v3
	global_store_short v3, v2, s[0:1] sc1
	s_waitcnt lgkmcnt(0)
	v_cvt_f16_f32_e32 v0, v0
	v_or_b32_e32 v2, s7, v37
	v_lshlrev_b32_e32 v2, 9, v2
	v_or3_b32 v2, v17, v2, s6
	v_lshlrev_b32_e32 v2, 1, v2
	global_store_short v2, v0, s[0:1] sc1
	v_cvt_f16_f32_e32 v2, v1
	ds_read2_b32 v[0:1], v4 offset0:56 offset1:60
	v_or_b32_e32 v3, s7, v38
	v_lshlrev_b32_e32 v3, 9, v3
	v_or3_b32 v3, v17, v3, s6
	v_lshlrev_b32_e32 v3, 1, v3
	global_store_short v3, v2, s[0:1] sc1
	s_waitcnt lgkmcnt(0)
	v_cvt_f16_f32_e32 v0, v0
	v_or_b32_e32 v2, s7, v39
	v_lshlrev_b32_e32 v2, 9, v2
	v_or3_b32 v2, v17, v2, s6
	v_lshlrev_b32_e32 v2, 1, v2
	global_store_short v2, v0, s[0:1] sc1
	v_cvt_f16_f32_e32 v0, v1
	v_or_b32_e32 v1, s7, v40
	v_lshlrev_b32_e32 v1, 9, v1
	v_or3_b32 v1, v17, v1, s6
	v_lshlrev_b32_e32 v1, 1, v1
	global_store_short v1, v0, s[0:1] sc1
	s_endpgm
.LBB0_37:
	v_ashrrev_i32_e32 v3, 31, v2
	v_lshl_add_u64 v[6:7], v[2:3], 2, s[22:23]
	v_add_u32_e32 v2, 1, v2
	global_store_dword v[6:7], v4, off sc1
	s_or_b64 exec, exec, s[30:31]
	s_and_saveexec_b64 s[18:19], s[16:17]
	s_cbranch_execz .LBB0_22
.LBB0_38:
	v_ashrrev_i32_e32 v3, 31, v2
	v_lshl_add_u64 v[6:7], v[2:3], 2, s[22:23]
	v_add_u32_e32 v2, 1, v2
	v_or_b32_e32 v1, 1, v4
	global_store_dword v[6:7], v1, off sc1
	s_or_b64 exec, exec, s[18:19]
	s_and_saveexec_b64 s[16:17], s[14:15]
	s_cbranch_execz .LBB0_23
.LBB0_39:
	v_ashrrev_i32_e32 v3, 31, v2
	v_lshl_add_u64 v[6:7], v[2:3], 2, s[22:23]
	v_add_u32_e32 v2, 1, v2
	v_or_b32_e32 v1, 2, v4
	global_store_dword v[6:7], v1, off sc1
	s_or_b64 exec, exec, s[16:17]
	s_and_saveexec_b64 s[14:15], s[12:13]
	s_cbranch_execz .LBB0_24
.LBB0_40:
	v_ashrrev_i32_e32 v3, 31, v2
	v_lshl_add_u64 v[6:7], v[2:3], 2, s[22:23]
	v_add_u32_e32 v2, 1, v2
	v_or_b32_e32 v1, 3, v4
	global_store_dword v[6:7], v1, off sc1
	s_or_b64 exec, exec, s[14:15]
	s_and_saveexec_b64 s[12:13], s[10:11]
	s_cbranch_execz .LBB0_25
.LBB0_41:
	v_ashrrev_i32_e32 v3, 31, v2
	v_lshl_add_u64 v[6:7], v[2:3], 2, s[22:23]
	v_add_u32_e32 v2, 1, v2
	v_or_b32_e32 v1, 4, v4
	global_store_dword v[6:7], v1, off sc1
	s_or_b64 exec, exec, s[12:13]
	s_and_saveexec_b64 s[10:11], s[8:9]
	s_cbranch_execz .LBB0_26
.LBB0_42:
	v_ashrrev_i32_e32 v3, 31, v2
	v_lshl_add_u64 v[6:7], v[2:3], 2, s[22:23]
	v_add_u32_e32 v2, 1, v2
	v_or_b32_e32 v1, 5, v4
	global_store_dword v[6:7], v1, off sc1
	s_or_b64 exec, exec, s[10:11]
	s_and_saveexec_b64 s[8:9], s[6:7]
	s_cbranch_execz .LBB0_27
.LBB0_43:
	v_ashrrev_i32_e32 v3, 31, v2
	v_lshl_add_u64 v[6:7], v[2:3], 2, s[22:23]
	v_add_u32_e32 v2, 1, v2
	v_or_b32_e32 v1, 6, v4
	global_store_dword v[6:7], v1, off sc1
	s_or_b64 exec, exec, s[8:9]
	s_and_saveexec_b64 s[6:7], s[4:5]
	s_cbranch_execz .LBB0_28
.LBB0_44:
	v_ashrrev_i32_e32 v3, 31, v2
	v_lshl_add_u64 v[2:3], v[2:3], 2, s[22:23]
	v_or_b32_e32 v1, 7, v4
	global_store_dword v[2:3], v1, off sc1
	s_or_b64 exec, exec, s[6:7]
	s_and_saveexec_b64 s[4:5], s[20:21]
	s_cbranch_execnz .LBB0_29
	s_branch .LBB0_30
	.p2align	8

_ZN12_GLOBAL__N_110qkv_kernelEPKfPKDF16_S1_S1_S1_PKiS5_S1_PDF16_S6_S6_:
	s_cmpk_lt_u32 s2, 0x200
	s_cbranch_scc0 .Lmy_noremap
	s_xor_b32 s2, s2, 0x100
.Lmy_noremap:
	s_load_dwordx2 s[26:27], s[0:1], 0x50
	s_cmpk_gt_i32 s2, 0xff
	s_cbranch_scc0 .LBB1_9
	s_load_dwordx2 s[4:5], s[0:1], 0x30
	s_add_i32 s3, s2, 0xffffff00
	s_lshr_b32 s3, s3, 3
	s_and_b32 s6, s2, 4
	s_and_b32 s3, s3, 0x1ffffff8
	s_or_b32 s3, s3, s6
	s_and_b32 s28, s2, 3
	s_lshr_b32 s8, s3, 2
	s_lshl_b32 s3, s28, 2
	s_waitcnt lgkmcnt(0)
	s_load_dword s10, s[4:5], s3 offset:0x0
	s_lshr_b32 s7, s2, 3
	s_bfe_u32 s4, s7, 0x10002
	s_mul_i32 s33, s8, 0xa0
	s_bfe_u32 s3, s2, 0x30003
	s_add_i32 s36, s4, 1
	s_waitcnt lgkmcnt(0)
	s_cmp_lt_i32 s33, s10
	s_cselect_b64 s[4:5], -1, 0
	s_cmp_ge_i32 s33, s10
	s_mov_b64 s[6:7], -1
	s_cbranch_scc0 .LBB1_6
	s_add_i32 s6, s10, 0x9f
	s_mul_hi_i32 s6, s6, 0x66666667
	s_lshr_b32 s7, s6, 31
	s_ashr_i32 s6, s6, 6
	s_add_i32 s12, s6, s7
	s_add_i32 s6, s10, 63
	s_mul_i32 s9, s12, 0xa0
	s_and_b32 s6, s6, 0xfffffc0
	s_sub_i32 s6, s6, s9
	s_lshl_b32 s11, s6, 4
	s_cmp_eq_u32 s36, 2
	s_cselect_b64 s[6:7], -1, 0
	s_cmp_eq_u32 s8, s12
	s_cselect_b64 s[12:13], -1, 0
	s_and_b64 s[6:7], s[6:7], s[12:13]
	v_cmp_gt_i32_e32 vcc, s11, v0
	s_and_b64 s[12:13], s[6:7], vcc
	s_and_saveexec_b64 s[6:7], s[12:13]
	s_cbranch_execz .LBB1_5
	s_lshl_b32 s12, s3, 1
	s_lshl_b32 s13, s28, 3
	s_add_i32 s12, s13, s12
	s_add_i32 s12, s12, -8
	v_lshrrev_b32_e32 v2, 1, v0
	v_and_or_b32 v1, v0, 1, s12
	v_lshlrev_b32_e32 v4, 3, v2
	v_lshlrev_b32_e32 v5, 9, v2
	s_mulk_i32 s8, 0x1400
	v_lshrrev_b32_e32 v2, 4, v0
	v_mov_b32_e32 v3, 0
	v_mul_i32_i24_e32 v1, 36, v1
	v_lshl_or_b32 v6, v2, 5, s8
	v_add_u32_e32 v7, s9, v2
	s_mov_b64 s[8:9], 0
	v_mov_b32_e32 v10, v3
	v_mov_b32_e32 v11, v3
	v_mov_b32_e32 v12, v3
	v_mov_b32_e32 v13, v3
	v_mov_b32_e32 v8, v0

_ZN12_GLOBAL__N_111attn_kernelEPKDF16_S1_S1_PKiPDF16_:
	s_load_dwordx8 s[4:11], s[0:1], 0x0
	s_lshr_b32 s68, s2, 6
	s_and_b32 s33, s2, 7
	s_bfe_u32 s83, s2, 0x30003
	s_lshl_b32 s2, s68, 2
	s_waitcnt lgkmcnt(0)
	s_load_dword s64, s[10:11], s2 offset:0x0
	s_mov_b32 s69, 0
	s_lshl_b32 s2, s68, 3
	s_or_b32 s2, s2, s33
	v_readfirstlane_b32 s66, v0
	s_mov_b32 s3, s69
	s_lshl_b64 s[10:11], s[2:3], 6
	s_lshl_b32 s3, s83, 3
	s_lshr_b32 s82, s66, 6
	s_or_b32 s3, s10, s3
	s_add_u32 s10, s3, s82
	s_addc_u32 s11, s11, 0
	s_lshl_b64 s[10:11], s[10:11], 12
	s_add_u32 s4, s4, s10
	s_addc_u32 s5, s5, s11
	s_mul_hi_u32 s3, s2, 0x48000
	s_mul_i32 s2, s2, 0x48000
	s_add_u32 s6, s6, s2
	s_addc_u32 s7, s7, s3
	s_lshl_b32 s65, s82, 10
	s_add_u32 s74, s6, s65
	s_addc_u32 s75, s7, 0
	s_add_u32 s2, s8, s2
	s_addc_u32 s3, s9, s3
	s_add_u32 s72, s2, s65
	s_addc_u32 s73, s3, 0
	s_cmp_lg_u32 0, -1
	v_and_b32_e32 v198, 63, v0
	s_cselect_b32 s2, 0, 0
	v_bfe_u32 v200, v0, 5, 1
	v_lshlrev_b32_e32 v205, 4, v198
	s_add_i32 s88, s65, s2
	s_mov_b32 s2, m0
	s_mov_b32 m0, s88
	s_nop 0
	global_load_lds_dwordx4 v205, s[74:75]
	s_mov_b32 m0, s2
	v_and_b32_e32 v199, 31, v0
	s_add_i32 s87, s88, 0x6000
	s_mov_b32 s2, m0
	s_mov_b32 m0, s87
	s_nop 0
	global_load_lds_dwordx4 v205, s[72:73]
	s_mov_b32 m0, s2
	v_lshlrev_b32_e32 v196, 9, v200
	v_mov_b32_e32 v197, 0
	v_lshlrev_b32_e32 v18, 4, v199
	s_add_u32 s2, s74, 0x2000
	v_lshl_add_u64 v[2:3], s[4:5], 0, v[196:197]
	v_mov_b32_e32 v19, v197
	s_addc_u32 s3, s75, 0
	s_add_i32 s6, s88, 0x2000
	s_mov_b32 s7, m0
	s_mov_b32 m0, s6
	s_nop 0
	global_load_lds_dwordx4 v205, s[2:3]
	s_mov_b32 m0, s7
	v_lshl_add_u64 v[12:13], v[2:3], 0, v[18:19]
	global_load_dwordx4 v[140:143], v[12:13], off
	global_load_dwordx4 v[136:139], v[12:13], off offset:1024
	global_load_dwordx4 v[132:135], v[12:13], off offset:2048
	global_load_dwordx4 v[128:131], v[12:13], off offset:3072
	v_mov_b32_e32 v2, v197
	v_mov_b32_e32 v3, v197
	v_mov_b32_e32 v4, v197
	v_mov_b32_e32 v5, v197
	v_mov_b32_e32 v6, v197
	v_mov_b32_e32 v7, v197
	v_mov_b32_e32 v8, v197
	v_mov_b32_e32 v9, v197
	v_mov_b32_e32 v10, v197
	v_mov_b32_e32 v11, v197
	v_mov_b32_e32 v12, v197
	v_mov_b32_e32 v13, v197
	v_mov_b32_e32 v14, v197
	v_mov_b32_e32 v15, v197
	v_mov_b32_e32 v16, v197
	v_mov_b32_e32 v17, v197
	s_add_u32 s2, s74, 0x4000
	v_lshlrev_b32_e32 v1, 10, v200
	s_addc_u32 s3, s75, 0
	s_add_i32 s4, s88, 0x4000
	s_mov_b32 s5, m0
	s_mov_b32 m0, s4
	s_nop 0
	global_load_lds_dwordx4 v205, s[2:3]
	s_mov_b32 m0, s5
	v_add3_u32 v207, 0, v1, v18
	s_waitcnt vmcnt(3) lgkmcnt(0)
	s_barrier
	s_add_i32 s100, s64, 63
	s_ashr_i32 s101, s100, 31
	s_lshr_b32 s101, s101, 26
	s_add_i32 s100, s100, s101
	s_ashr_i32 s89, s100, 6
	s_add_i32 s86, s89, -1
	s_lshl_b32 s100, s86, 6
	s_sub_i32 s85, s64, s100
	ds_read_b128 v[34:37], v207
	ds_read_b128 v[38:41], v207 offset:512
	s_add_i32 s2, s64, -1
	v_lshlrev_b32_e32 v1, 8, v200
	s_movk_i32 s90, 0x2000
	s_mov_b64 s[76:77], 0x4000
	s_movk_i32 s80, 0x4000
	s_cmp_gt_u32 s2, 63
	s_waitcnt vmcnt(3) lgkmcnt(1)
	v_mfma_f32_32x32x16_f16 v[18:33], v[34:37], v[140:143], v[2:17]
	s_waitcnt lgkmcnt(0)
	v_mfma_f32_32x32x16_f16 v[2:17], v[38:41], v[140:143], v[2:17]
	ds_read_b128 v[34:37], v207 offset:2048
	ds_read_b128 v[38:41], v207 offset:2560
	s_waitcnt vmcnt(2) lgkmcnt(1)
	v_mfma_f32_32x32x16_f16 v[18:33], v[34:37], v[136:139], v[18:33]
	s_waitcnt lgkmcnt(0)
	v_mfma_f32_32x32x16_f16 v[2:17], v[38:41], v[136:139], v[2:17]
	ds_read_b128 v[34:37], v207 offset:4096
	ds_read_b128 v[38:41], v207 offset:4608
	s_waitcnt vmcnt(1) lgkmcnt(1)
	v_mfma_f32_32x32x16_f16 v[18:33], v[34:37], v[132:135], v[18:33]
	s_waitcnt lgkmcnt(0)
	v_mfma_f32_32x32x16_f16 v[2:17], v[38:41], v[132:135], v[2:17]
	ds_read_b128 v[34:37], v207 offset:6144
	ds_read_b128 v[38:41], v207 offset:6656
	s_waitcnt vmcnt(0) lgkmcnt(1)
	v_mfma_f32_32x32x16_f16 v[18:33], v[34:37], v[128:131], v[18:33]
	s_waitcnt lgkmcnt(0)
	v_mfma_f32_32x32x16_f16 v[2:17], v[38:41], v[128:131], v[2:17]
	s_nop 15
	s_nop 7
	s_cbranch_scc1 .LBB3_2
	v_lshlrev_b32_e32 v34, 2, v200
	v_or_b32_e32 v35, 32, v34
	v_cmp_gt_i32_e32 vcc, s85, v35
	v_or_b32_e32 v35, 1, v34
	v_cmp_gt_i32_e64 s[30:31], s85, v35
	v_or_b32_e32 v35, 33, v34
	v_cmp_gt_i32_e64 s[2:3], s85, v35
	v_or_b32_e32 v35, 2, v34
	v_cmp_gt_i32_e64 s[36:37], s85, v35
	v_or_b32_e32 v35, 34, v34
	v_cmp_gt_i32_e64 s[4:5], s85, v35
	v_or_b32_e32 v35, 3, v34
	v_cmp_gt_i32_e64 s[38:39], s85, v35
	v_or_b32_e32 v35, 35, v34
	v_cmp_gt_i32_e64 s[6:7], s85, v35
	v_or_b32_e32 v35, 8, v34
	v_cmp_gt_i32_e64 s[40:41], s85, v35
	v_or_b32_e32 v35, 40, v34
	v_cmp_gt_i32_e64 s[8:9], s85, v35
	v_or_b32_e32 v35, 9, v34
	v_cmp_gt_i32_e64 s[42:43], s85, v35
	v_or_b32_e32 v35, 41, v34
	v_cmp_gt_i32_e64 s[10:11], s85, v35
	v_or_b32_e32 v35, 10, v34
	v_cmp_gt_i32_e64 s[44:45], s85, v35
	v_or_b32_e32 v35, 42, v34
	v_cmp_gt_i32_e64 s[12:13], s85, v35
	v_or_b32_e32 v35, 11, v34
	v_cmp_gt_i32_e64 s[46:47], s85, v35
	v_or_b32_e32 v35, 43, v34
	v_cmp_gt_i32_e64 s[14:15], s85, v35
	v_or_b32_e32 v35, 16, v34
	v_cmp_gt_i32_e64 s[48:49], s85, v35
	v_or_b32_e32 v35, 48, v34
	v_cmp_gt_i32_e64 s[16:17], s85, v35
	v_or_b32_e32 v35, 17, v34
	v_cmp_gt_i32_e64 s[50:51], s85, v35
	v_or_b32_e32 v35, 49, v34
	v_cmp_gt_i32_e64 s[18:19], s85, v35
	v_or_b32_e32 v35, 18, v34
	v_cmp_gt_i32_e64 s[52:53], s85, v35
	v_or_b32_e32 v35, 50, v34
	v_cmp_gt_i32_e64 s[20:21], s85, v35
	v_or_b32_e32 v35, 19, v34
	v_cmp_gt_i32_e64 s[54:55], s85, v35
	v_or_b32_e32 v35, 51, v34
	v_cmp_gt_i32_e64 s[22:23], s85, v35
	v_or_b32_e32 v35, 24, v34
	v_cmp_gt_i32_e64 s[56:57], s85, v35
	v_or_b32_e32 v35, 56, v34
	v_cmp_gt_i32_e64 s[24:25], s85, v35
	v_or_b32_e32 v35, 25, v34
	v_cmp_gt_i32_e64 s[58:59], s85, v35
	v_or_b32_e32 v35, 57, v34
	v_cmp_gt_i32_e64 s[28:29], s85, v35
	v_or_b32_e32 v35, 26, v34
	v_cmp_gt_i32_e64 s[60:61], s85, v35
	v_or_b32_e32 v35, 58, v34
	v_cmp_gt_i32_e64 s[34:35], s85, v35
	v_or_b32_e32 v35, 27, v34
	v_cmp_gt_i32_e64 s[62:63], s85, v35
	s_or_b64 s[60:61], s[62:63], s[60:61]
	s_or_b64 s[58:59], s[60:61], s[58:59]
	s_or_b64 s[56:57], s[58:59], s[56:57]
	s_or_b64 s[54:55], s[56:57], s[54:55]
	s_or_b64 s[52:53], s[54:55], s[52:53]
	s_or_b64 s[50:51], s[52:53], s[50:51]
	s_or_b64 s[48:49], s[50:51], s[48:49]
	s_or_b64 s[46:47], s[48:49], s[46:47]
	s_or_b64 s[44:45], s[46:47], s[44:45]
	s_or_b64 s[42:43], s[44:45], s[42:43]
	s_or_b64 s[40:41], s[42:43], s[40:41]
	s_or_b64 s[38:39], s[40:41], s[38:39]
	s_or_b64 s[36:37], s[38:39], s[36:37]
	v_cmp_gt_i32_e64 s[26:27], s85, v34
	s_or_b64 s[30:31], s[36:37], s[30:31]
	v_mov_b32_e32 v36, 0xff800000
	s_or_b64 s[26:27], s[30:31], s[26:27]
	v_or_b32_e32 v34, 59, v34
	v_cndmask_b32_e64 v18, v36, v18, s[26:27]
	v_cmp_gt_i32_e64 s[26:27], s85, v34
	v_cndmask_b32_e64 v33, v36, v33, s[62:63]
	v_cndmask_b32_e64 v32, v36, v32, s[60:61]
	v_cndmask_b32_e64 v17, v36, v17, s[26:27]
	s_or_b64 s[26:27], s[26:27], s[34:35]
	v_cndmask_b32_e64 v16, v36, v16, s[26:27]
	s_or_b64 s[26:27], s[26:27], s[28:29]
	s_or_b64 s[24:25], s[26:27], s[24:25]
	s_or_b64 s[22:23], s[24:25], s[22:23]
	s_or_b64 s[20:21], s[22:23], s[20:21]
	s_or_b64 s[18:19], s[20:21], s[18:19]
	s_or_b64 s[16:17], s[18:19], s[16:17]
	s_or_b64 s[14:15], s[16:17], s[14:15]
	s_or_b64 s[12:13], s[14:15], s[12:13]
	s_or_b64 s[10:11], s[12:13], s[10:11]
	s_or_b64 s[8:9], s[10:11], s[8:9]
	s_or_b64 s[6:7], s[8:9], s[6:7]
	s_or_b64 s[4:5], s[6:7], s[4:5]
	s_or_b64 s[2:3], s[4:5], s[2:3]
	s_or_b64 vcc, s[2:3], vcc
	v_cndmask_b32_e64 v31, v36, v31, s[58:59]
	v_cndmask_b32_e64 v30, v36, v30, s[56:57]
	v_cndmask_b32_e64 v29, v36, v29, s[54:55]
	v_cndmask_b32_e64 v28, v36, v28, s[52:53]
	v_cndmask_b32_e64 v27, v36, v27, s[50:51]
	v_cndmask_b32_e64 v26, v36, v26, s[48:49]
	v_cndmask_b32_e64 v25, v36, v25, s[46:47]
	v_cndmask_b32_e64 v24, v36, v24, s[44:45]
	v_cndmask_b32_e64 v23, v36, v23, s[42:43]
	v_cndmask_b32_e64 v22, v36, v22, s[40:41]
	v_cndmask_b32_e64 v21, v36, v21, s[38:39]
	v_cndmask_b32_e64 v20, v36, v20, s[36:37]
	v_cndmask_b32_e64 v19, v36, v19, s[30:31]
	v_cndmask_b32_e64 v15, v36, v15, s[26:27]
	v_cndmask_b32_e64 v14, v36, v14, s[24:25]
	v_cndmask_b32_e64 v13, v36, v13, s[22:23]
	v_cndmask_b32_e64 v12, v36, v12, s[20:21]
	v_cndmask_b32_e64 v11, v36, v11, s[18:19]
	v_cndmask_b32_e64 v10, v36, v10, s[16:17]
	v_cndmask_b32_e64 v9, v36, v9, s[14:15]
	v_cndmask_b32_e64 v8, v36, v8, s[12:13]
	v_cndmask_b32_e64 v7, v36, v7, s[10:11]
	v_cndmask_b32_e64 v6, v36, v6, s[8:9]
	v_cndmask_b32_e64 v5, v36, v5, s[6:7]
	v_cndmask_b32_e64 v4, v36, v4, s[4:5]
	v_cndmask_b32_e64 v3, v36, v3, s[2:3]
	v_cndmask_b32_e32 v2, v36, v2, vcc

.LBB3_4:
	v_add_u32_e32 v65, s0, v208
	ds_read_b64_tr_b16 v[192:193], v65 offset:24576
	ds_read_b64_tr_b16 v[194:195], v65 offset:25088
	s_waitcnt lgkmcnt(2)
	v_mfma_f32_32x32x16_f16 v[112:127], v[188:191], v[140:143], v[32:47]
	v_add_f32_e32 v66, v48, v49
	v_add_f32_e32 v66, v50, v66
	v_add_f32_e32 v66, v51, v66
	v_add_f32_e32 v66, v52, v66
	v_add_f32_e32 v66, v53, v66
	v_cvt_pk_f16_f32 v156, v48, v49
	v_cvt_pk_f16_f32 v157, v50, v51
	ds_read_b64_tr_b16 v[74:75], v65 offset:28672
	ds_read_b64_tr_b16 v[76:77], v65 offset:29184
	v_mfma_f32_32x32x16_f16 v[96:111], v[184:187], v[140:143], v[32:47]
	v_add_f32_e32 v48, v54, v66
	v_add_f32_e32 v48, v55, v48
	v_add_f32_e32 v48, v56, v48
	v_add_f32_e32 v48, v57, v48
	v_cvt_pk_f16_f32 v158, v52, v53
	v_cvt_pk_f16_f32 v159, v54, v55
	ds_read_b64_tr_b16 v[70:71], v65 offset:25600
	ds_read_b64_tr_b16 v[72:73], v65 offset:26112
	v_mfma_f32_32x32x16_f16 v[112:127], v[180:183], v[136:139], v[112:127]
	v_add_f32_e32 v48, v58, v48
	v_add_f32_e32 v48, v59, v48
	v_add_f32_e32 v48, v60, v48
	v_add_f32_e32 v48, v61, v48
	v_cvt_pk_f16_f32 v152, v56, v57
	v_cvt_pk_f16_f32 v153, v58, v59
	ds_read_b64_tr_b16 v[66:67], v65 offset:29696
	ds_read_b64_tr_b16 v[68:69], v65 offset:30208
	v_mfma_f32_32x32x16_f16 v[96:111], v[176:179], v[136:139], v[96:111]
	v_add_f32_e32 v48, v62, v48
	v_add_f32_e32 v48, v63, v48
	v_add_f32_e32 v48, v80, v48
	v_add_f32_e32 v48, v81, v48
	v_cvt_pk_f16_f32 v154, v60, v61
	v_cvt_pk_f16_f32 v155, v62, v63
	ds_read_b64_tr_b16 v[60:61], v65 offset:26624
	ds_read_b64_tr_b16 v[62:63], v65 offset:27136
	v_mfma_f32_32x32x16_f16 v[112:127], v[172:175], v[132:135], v[112:127]
	v_add_f32_e32 v48, v82, v48
	v_add_f32_e32 v48, v83, v48
	v_add_f32_e32 v48, v84, v48
	v_add_f32_e32 v48, v85, v48
	v_cvt_pk_f16_f32 v148, v80, v81
	v_cvt_pk_f16_f32 v149, v82, v83
	ds_read_b64_tr_b16 v[56:57], v65 offset:30720
	ds_read_b64_tr_b16 v[58:59], v65 offset:31232
	v_mfma_f32_32x32x16_f16 v[96:111], v[168:171], v[132:135], v[96:111]
	v_add_f32_e32 v48, v86, v48
	v_add_f32_e32 v48, v87, v48
	v_add_f32_e32 v48, v88, v48
	v_add_f32_e32 v48, v89, v48
	v_cvt_pk_f16_f32 v150, v84, v85
	v_cvt_pk_f16_f32 v151, v86, v87
	ds_read_b64_tr_b16 v[52:53], v65 offset:27648
	ds_read_b64_tr_b16 v[54:55], v65 offset:28160
	v_mfma_f32_32x32x16_f16 v[112:127], v[164:167], v[128:131], v[112:127]
	v_add_f32_e32 v48, v90, v48
	v_add_f32_e32 v48, v91, v48
	v_add_f32_e32 v48, v92, v48
	v_add_f32_e32 v78, v93, v48
	v_cvt_pk_f16_f32 v144, v88, v89
	v_cvt_pk_f16_f32 v145, v90, v91
	ds_read_b64_tr_b16 v[48:49], v65 offset:31744
	ds_read_b64_tr_b16 v[50:51], v65 offset:32256
	v_mfma_f32_32x32x16_f16 v[96:111], v[160:163], v[128:131], v[96:111]
	v_add_f32_e32 v65, v94, v78
	v_add_f32_e32 v65, v95, v65
	v_add_f32_e32 v65, 0, v65
	v_cvt_pk_f16_f32 v146, v92, v93
	v_cvt_pk_f16_f32 v147, v94, v95
	s_add_u32 s97, s74, s76
	s_addc_u32 s98, s75, s77
	s_add_u32 s0, s97, 0x8000
	s_addc_u32 s1, s98, 0
	s_add_i32 s78, s96, s88
	s_add_u32 s99, s72, s76
	s_mov_b32 s79, m0
	s_mov_b32 m0, s78
	s_nop 0
	global_load_lds_dwordx4 v205, s[0:1]
	s_mov_b32 m0, s79
	s_addc_u32 s0, s73, s77
	s_add_u32 s78, s99, 0x4000
	s_addc_u32 s79, s0, 0
	s_add_i32 s1, s92, s87
	s_mov_b32 s80, m0
	s_mov_b32 m0, s1
	s_nop 0
	global_load_lds_dwordx4 v205, s[78:79]
	s_mov_b32 m0, s80
	s_cmp_lg_u32 s94, s91
	s_cbranch_scc1 .LBB3_6
	s_or_b64 vcc, s[64:65], s[60:61]
	v_cndmask_b32_e32 v126, v209, v126, vcc
	s_or_b64 vcc, vcc, s[56:57]
	v_cndmask_b32_e32 v125, v209, v125, vcc
	s_or_b64 vcc, vcc, s[52:53]
	v_cndmask_b32_e32 v124, v209, v124, vcc
	s_or_b64 vcc, vcc, s[48:49]
	v_cndmask_b32_e32 v123, v209, v123, vcc
	s_or_b64 vcc, vcc, s[44:45]
	v_cndmask_b32_e32 v122, v209, v122, vcc
	s_or_b64 vcc, vcc, s[40:41]
	v_cndmask_b32_e32 v121, v209, v121, vcc
	s_or_b64 vcc, vcc, s[36:37]
	v_cndmask_b32_e32 v120, v209, v120, vcc
	s_or_b64 vcc, vcc, s[30:31]
	v_cndmask_b32_e32 v119, v209, v119, vcc
	s_or_b64 vcc, vcc, s[26:27]
	v_cndmask_b32_e32 v118, v209, v118, vcc
	s_or_b64 vcc, vcc, s[22:23]
	v_cndmask_b32_e32 v117, v209, v117, vcc
	s_or_b64 vcc, vcc, s[18:19]
	v_cndmask_b32_e32 v116, v209, v116, vcc
	s_or_b64 vcc, vcc, s[14:15]
	v_cndmask_b32_e32 v115, v209, v115, vcc
	s_or_b64 vcc, vcc, s[10:11]
	v_cndmask_b32_e32 v114, v209, v114, vcc
	s_or_b64 vcc, vcc, s[6:7]
	v_cndmask_b32_e32 v113, v209, v113, vcc
	s_or_b64 vcc, vcc, s[2:3]
	v_cndmask_b32_e32 v112, v209, v112, vcc
	s_or_b64 vcc, s[66:67], s[62:63]
	v_cndmask_b32_e32 v110, v209, v110, vcc
	s_or_b64 vcc, vcc, s[58:59]
	v_cndmask_b32_e32 v109, v209, v109, vcc
	s_or_b64 vcc, vcc, s[54:55]
	v_cndmask_b32_e32 v108, v209, v108, vcc
	s_or_b64 vcc, vcc, s[50:51]
	v_cndmask_b32_e32 v107, v209, v107, vcc
	s_or_b64 vcc, vcc, s[46:47]
	v_cndmask_b32_e32 v106, v209, v106, vcc
	s_or_b64 vcc, vcc, s[42:43]
	v_cndmask_b32_e32 v105, v209, v105, vcc
	s_or_b64 vcc, vcc, s[38:39]
	v_cndmask_b32_e32 v104, v209, v104, vcc
	s_or_b64 vcc, vcc, s[34:35]
	v_cndmask_b32_e32 v103, v209, v103, vcc
	s_or_b64 vcc, vcc, s[28:29]
	v_cndmask_b32_e32 v102, v209, v102, vcc
	s_or_b64 vcc, vcc, s[24:25]
	v_cndmask_b32_e32 v101, v209, v101, vcc
	s_or_b64 vcc, vcc, s[20:21]
	v_cndmask_b32_e32 v100, v209, v100, vcc
	s_or_b64 vcc, vcc, s[16:17]
	v_cndmask_b32_e32 v99, v209, v99, vcc
	s_or_b64 vcc, vcc, s[12:13]
	v_cndmask_b32_e32 v98, v209, v98, vcc
	s_or_b64 vcc, vcc, s[8:9]
	v_cndmask_b32_e32 v97, v209, v97, vcc
	s_or_b64 vcc, vcc, s[4:5]
	v_cndmask_b32_e64 v127, v209, v127, s[64:65]
	v_cndmask_b32_e64 v111, v209, v111, s[66:67]
	v_cndmask_b32_e32 v96, v209, v96, vcc

.LBB3_7:
	s_waitcnt lgkmcnt(14)
	v_mfma_f32_32x32x16_f16 v[0:15], v[156:159], v[192:195], v[0:15]
	v_exp_f32_e32 v112, v112
	v_exp_f32_e32 v113, v113
	v_exp_f32_e32 v114, v114
	v_exp_f32_e32 v115, v115
	s_waitcnt lgkmcnt(12)
	v_mfma_f32_32x32x16_f16 v[16:31], v[156:159], v[74:77], v[16:31]
	v_exp_f32_e32 v116, v116
	v_exp_f32_e32 v117, v117
	v_exp_f32_e32 v118, v118
	v_exp_f32_e32 v119, v119
	v_add_u32_e32 v82, s92, v207
	ds_read_b128 v[78:81], v82
	ds_read_b128 v[160:163], v82 offset:512
	s_waitcnt lgkmcnt(12)
	v_mfma_f32_32x32x16_f16 v[0:15], v[152:155], v[70:73], v[0:15]
	v_exp_f32_e32 v120, v120
	v_exp_f32_e32 v121, v121
	v_exp_f32_e32 v122, v122
	v_exp_f32_e32 v123, v123
	ds_read_b128 v[180:183], v82 offset:2048
	ds_read_b128 v[70:73], v82 offset:2560
	s_waitcnt lgkmcnt(12)
	v_mfma_f32_32x32x16_f16 v[16:31], v[152:155], v[66:69], v[16:31]
	v_exp_f32_e32 v124, v124
	v_exp_f32_e32 v125, v125
	v_exp_f32_e32 v126, v126
	v_exp_f32_e32 v127, v127
	ds_read_b128 v[74:77], v82 offset:4096
	ds_read_b128 v[64:67], v82 offset:4608
	s_waitcnt lgkmcnt(12)
	v_mfma_f32_32x32x16_f16 v[0:15], v[148:151], v[60:63], v[0:15]
	v_exp_f32_e32 v96, v96
	v_exp_f32_e32 v97, v97
	v_exp_f32_e32 v98, v98
	v_exp_f32_e32 v99, v99
	ds_read_b128 v[176:179], v82 offset:6144
	ds_read_b128 v[172:175], v82 offset:6656
	s_waitcnt lgkmcnt(12)
	v_mfma_f32_32x32x16_f16 v[16:31], v[148:151], v[56:59], v[16:31]
	v_exp_f32_e32 v100, v100
	v_exp_f32_e32 v101, v101
	v_exp_f32_e32 v102, v102
	v_exp_f32_e32 v103, v103
	s_waitcnt lgkmcnt(10)
	v_mfma_f32_32x32x16_f16 v[0:15], v[144:147], v[52:55], v[0:15]
	v_exp_f32_e32 v104, v104
	v_exp_f32_e32 v105, v105
	v_exp_f32_e32 v106, v106
	v_exp_f32_e32 v107, v107
	s_waitcnt lgkmcnt(8)
	v_mfma_f32_32x32x16_f16 v[16:31], v[144:147], v[48:51], v[16:31]
	v_exp_f32_e32 v108, v108
	v_exp_f32_e32 v109, v109
	v_exp_f32_e32 v110, v110
	v_exp_f32_e32 v111, v111
	s_waitcnt vmcnt(2) lgkmcnt(0)
	s_barrier
	s_andn2_b64 vcc, exec, s[78:79]
	s_cbranch_vccnz .LBB3_9
	s_waitcnt lgkmcnt(0)
	ds_read_b128 v[48:51], v210 offset:49248
	ds_read_b128 v[52:55], v210 offset:49216
	ds_read_b128 v[56:59], v210 offset:49184
	ds_read_b128 v[60:63], v210 offset:49152
	s_waitcnt lgkmcnt(3)
	v_pk_mul_f32 v[12:13], v[12:13], v[48:49]
	s_waitcnt lgkmcnt(2)
	v_pk_mul_f32 v[8:9], v[8:9], v[52:53]
	s_waitcnt lgkmcnt(1)
	v_pk_mul_f32 v[4:5], v[4:5], v[56:57]
	v_pk_mul_f32 v[14:15], v[14:15], v[50:51]
	v_pk_mul_f32 v[10:11], v[10:11], v[54:55]
	v_pk_mul_f32 v[6:7], v[6:7], v[58:59]
	s_waitcnt lgkmcnt(0)
	v_pk_mul_f32 v[2:3], v[2:3], v[62:63]
	v_pk_mul_f32 v[0:1], v[0:1], v[60:61]
	v_pk_mul_f32 v[28:29], v[28:29], v[48:49]
	v_pk_mul_f32 v[24:25], v[24:25], v[52:53]
	v_pk_mul_f32 v[20:21], v[20:21], v[56:57]
	v_pk_mul_f32 v[30:31], v[30:31], v[50:51]
	v_pk_mul_f32 v[26:27], v[26:27], v[54:55]
	v_pk_mul_f32 v[22:23], v[22:23], v[58:59]
	v_pk_mul_f32 v[18:19], v[18:19], v[62:63]
	v_pk_mul_f32 v[16:17], v[16:17], v[60:61]

.LBB3_25:
	v_add_u32_e32 v65, s92, v208
	ds_read_b64_tr_b16 v[192:193], v65 offset:24576
	ds_read_b64_tr_b16 v[194:195], v65 offset:25088
	s_waitcnt lgkmcnt(2)
	v_mfma_f32_32x32x16_f16 v[96:111], v[188:191], v[140:143], v[32:47]
	v_add_f32_e32 v66, v48, v49
	v_add_f32_e32 v66, v50, v66
	v_add_f32_e32 v66, v51, v66
	v_add_f32_e32 v66, v52, v66
	v_add_f32_e32 v66, v53, v66
	v_cvt_pk_f16_f32 v156, v48, v49
	v_cvt_pk_f16_f32 v157, v50, v51
	ds_read_b64_tr_b16 v[188:189], v65 offset:28672
	ds_read_b64_tr_b16 v[190:191], v65 offset:29184
	v_mfma_f32_32x32x16_f16 v[32:47], v[184:187], v[140:143], v[32:47]
	v_add_f32_e32 v48, v54, v66
	v_add_f32_e32 v48, v55, v48
	v_add_f32_e32 v48, v56, v48
	v_add_f32_e32 v48, v57, v48
	v_cvt_pk_f16_f32 v158, v52, v53
	v_cvt_pk_f16_f32 v159, v54, v55
	ds_read_b64_tr_b16 v[124:125], v65 offset:25600
	ds_read_b64_tr_b16 v[126:127], v65 offset:26112
	v_mfma_f32_32x32x16_f16 v[96:111], v[180:183], v[136:139], v[96:111]
	v_add_f32_e32 v48, v58, v48
	v_add_f32_e32 v48, v59, v48
	v_add_f32_e32 v48, v60, v48
	v_add_f32_e32 v48, v61, v48
	v_cvt_pk_f16_f32 v152, v56, v57
	v_cvt_pk_f16_f32 v153, v58, v59
	ds_read_b64_tr_b16 v[120:121], v65 offset:29696
	ds_read_b64_tr_b16 v[122:123], v65 offset:30208
	v_mfma_f32_32x32x16_f16 v[32:47], v[176:179], v[136:139], v[32:47]
	v_add_f32_e32 v48, v62, v48
	v_add_f32_e32 v48, v63, v48
	v_add_f32_e32 v48, v80, v48
	v_add_f32_e32 v48, v81, v48
	v_cvt_pk_f16_f32 v154, v60, v61
	v_cvt_pk_f16_f32 v155, v62, v63
	ds_read_b64_tr_b16 v[116:117], v65 offset:26624
	ds_read_b64_tr_b16 v[118:119], v65 offset:27136
	v_mfma_f32_32x32x16_f16 v[96:111], v[172:175], v[132:135], v[96:111]
	v_add_f32_e32 v48, v82, v48
	v_add_f32_e32 v48, v83, v48
	v_add_f32_e32 v48, v84, v48
	v_add_f32_e32 v48, v85, v48
	v_cvt_pk_f16_f32 v148, v80, v81
	v_cvt_pk_f16_f32 v149, v82, v83
	ds_read_b64_tr_b16 v[112:113], v65 offset:30720
	ds_read_b64_tr_b16 v[114:115], v65 offset:31232
	v_mfma_f32_32x32x16_f16 v[32:47], v[168:171], v[132:135], v[32:47]
	v_add_f32_e32 v48, v86, v48
	v_add_f32_e32 v48, v87, v48
	v_add_f32_e32 v48, v88, v48
	v_add_f32_e32 v66, v89, v48
	v_cvt_pk_f16_f32 v150, v84, v85
	v_cvt_pk_f16_f32 v151, v86, v87
	ds_read_b64_tr_b16 v[82:83], v65 offset:27648
	ds_read_b64_tr_b16 v[84:85], v65 offset:28160
	v_mov_b64_e32 v[48:49], v[96:97]
	v_mov_b64_e32 v[50:51], v[98:99]
	v_mov_b64_e32 v[52:53], v[100:101]
	v_mov_b64_e32 v[54:55], v[102:103]
	v_mov_b64_e32 v[56:57], v[104:105]
	v_mov_b64_e32 v[58:59], v[106:107]
	v_mov_b64_e32 v[60:61], v[108:109]
	v_mov_b64_e32 v[62:63], v[110:111]
	v_add_f32_e32 v66, v90, v66
	v_add_f32_e32 v66, v91, v66
	v_mfma_f32_32x32x16_f16 v[48:63], v[164:167], v[128:131], v[48:63]
	v_add_f32_e32 v66, v92, v66
	v_add_f32_e32 v66, v93, v66
	v_cvt_pk_f16_f32 v144, v88, v89
	v_cvt_pk_f16_f32 v145, v90, v91
	ds_read_b64_tr_b16 v[96:97], v65 offset:31744
	ds_read_b64_tr_b16 v[98:99], v65 offset:32256
	v_mfma_f32_32x32x16_f16 v[32:47], v[160:163], v[128:131], v[32:47]
	v_add_f32_e32 v65, v94, v66
	v_add_f32_e32 v65, v95, v65
	v_add_f32_e32 v65, 0, v65
	v_cvt_pk_f16_f32 v146, v92, v93
	v_cvt_pk_f16_f32 v147, v94, v95
	s_mov_b32 s3, 0
	s_add_i32 s2, s0, 3
	s_lshl_b64 s[2:3], s[2:3], 13
	s_add_u32 s2, s74, s2
	s_addc_u32 s3, s75, s3
	s_add_i32 s1, s90, s88
	s_mov_b32 s4, m0
	s_mov_b32 m0, s1
	s_nop 0
	global_load_lds_dwordx4 v205, s[2:3]
	s_mov_b32 m0, s4
	s_add_u32 s2, s72, s76
	s_addc_u32 s3, s73, s77
	s_add_i32 s1, s80, s87
	s_cmp_lg_u32 s0, s86
	s_mov_b32 s0, m0
	s_mov_b32 m0, s1
	s_nop 0
	global_load_lds_dwordx4 v205, s[2:3]
	s_mov_b32 m0, s0
	s_cbranch_scc1 .LBB3_27
	v_lshlrev_b32_e32 v66, 2, v200
	v_or_b32_e32 v67, 32, v66
	v_cmp_gt_i32_e32 vcc, s85, v67
	v_or_b32_e32 v67, 1, v66
	v_cmp_gt_i32_e64 s[28:29], s85, v67
	v_or_b32_e32 v67, 33, v66
	v_cmp_gt_i32_e64 s[0:1], s85, v67
	v_or_b32_e32 v67, 2, v66
	v_cmp_gt_i32_e64 s[34:35], s85, v67
	v_or_b32_e32 v67, 34, v66
	v_cmp_gt_i32_e64 s[2:3], s85, v67
	v_or_b32_e32 v67, 3, v66
	v_cmp_gt_i32_e64 s[36:37], s85, v67
	v_or_b32_e32 v67, 35, v66
	v_cmp_gt_i32_e64 s[4:5], s85, v67
	v_or_b32_e32 v67, 8, v66
	v_cmp_gt_i32_e64 s[38:39], s85, v67
	v_or_b32_e32 v67, 40, v66
	v_cmp_gt_i32_e64 s[6:7], s85, v67
	v_or_b32_e32 v67, 9, v66
	v_cmp_gt_i32_e64 s[40:41], s85, v67
	v_or_b32_e32 v67, 41, v66
	v_cmp_gt_i32_e64 s[8:9], s85, v67
	v_or_b32_e32 v67, 10, v66
	v_cmp_gt_i32_e64 s[42:43], s85, v67
	v_or_b32_e32 v67, 42, v66
	v_cmp_gt_i32_e64 s[10:11], s85, v67
	v_or_b32_e32 v67, 11, v66
	v_cmp_gt_i32_e64 s[44:45], s85, v67
	v_or_b32_e32 v67, 43, v66
	v_cmp_gt_i32_e64 s[12:13], s85, v67
	v_or_b32_e32 v67, 16, v66
	v_cmp_gt_i32_e64 s[46:47], s85, v67
	v_or_b32_e32 v67, 48, v66
	v_cmp_gt_i32_e64 s[14:15], s85, v67
	v_or_b32_e32 v67, 17, v66
	v_cmp_gt_i32_e64 s[48:49], s85, v67
	v_or_b32_e32 v67, 49, v66
	v_cmp_gt_i32_e64 s[16:17], s85, v67
	v_or_b32_e32 v67, 18, v66
	v_cmp_gt_i32_e64 s[50:51], s85, v67
	v_or_b32_e32 v67, 50, v66
	v_cmp_gt_i32_e64 s[18:19], s85, v67
	v_or_b32_e32 v67, 19, v66
	v_cmp_gt_i32_e64 s[52:53], s85, v67
	v_or_b32_e32 v67, 51, v66
	v_cmp_gt_i32_e64 s[20:21], s85, v67
	v_or_b32_e32 v67, 24, v66
	v_cmp_gt_i32_e64 s[54:55], s85, v67
	v_or_b32_e32 v67, 56, v66
	v_cmp_gt_i32_e64 s[22:23], s85, v67
	v_or_b32_e32 v67, 25, v66
	v_cmp_gt_i32_e64 s[56:57], s85, v67
	v_or_b32_e32 v67, 57, v66
	v_cmp_gt_i32_e64 s[26:27], s85, v67
	v_or_b32_e32 v67, 26, v66
	v_cmp_gt_i32_e64 s[58:59], s85, v67
	v_or_b32_e32 v67, 58, v66
	v_cmp_gt_i32_e64 s[30:31], s85, v67
	v_or_b32_e32 v67, 27, v66
	v_cmp_gt_i32_e64 s[60:61], s85, v67
	s_or_b64 s[58:59], s[60:61], s[58:59]
	s_or_b64 s[56:57], s[58:59], s[56:57]
	s_or_b64 s[54:55], s[56:57], s[54:55]
	s_or_b64 s[52:53], s[54:55], s[52:53]
	s_or_b64 s[50:51], s[52:53], s[50:51]
	s_or_b64 s[48:49], s[50:51], s[48:49]
	s_or_b64 s[46:47], s[48:49], s[46:47]
	s_or_b64 s[44:45], s[46:47], s[44:45]
	s_or_b64 s[42:43], s[44:45], s[42:43]
	s_or_b64 s[40:41], s[42:43], s[40:41]
	s_or_b64 s[38:39], s[40:41], s[38:39]
	s_or_b64 s[36:37], s[38:39], s[36:37]
	s_or_b64 s[34:35], s[36:37], s[34:35]
	v_cmp_gt_i32_e64 s[24:25], s85, v66
	s_or_b64 s[28:29], s[34:35], s[28:29]
	v_mov_b32_e32 v68, 0xff800000
	s_or_b64 s[24:25], s[28:29], s[24:25]
	v_or_b32_e32 v66, 59, v66
	v_cndmask_b32_e64 v48, v68, v48, s[24:25]
	v_cmp_gt_i32_e64 s[24:25], s85, v66
	v_cndmask_b32_e64 v63, v68, v63, s[60:61]
	v_cndmask_b32_e64 v62, v68, v62, s[58:59]
	v_cndmask_b32_e64 v47, v68, v47, s[24:25]
	s_or_b64 s[24:25], s[24:25], s[30:31]
	v_cndmask_b32_e64 v46, v68, v46, s[24:25]
	s_or_b64 s[24:25], s[24:25], s[26:27]
	s_or_b64 s[22:23], s[24:25], s[22:23]
	s_or_b64 s[20:21], s[22:23], s[20:21]
	s_or_b64 s[18:19], s[20:21], s[18:19]
	s_or_b64 s[16:17], s[18:19], s[16:17]
	s_or_b64 s[14:15], s[16:17], s[14:15]
	s_or_b64 s[12:13], s[14:15], s[12:13]
	s_or_b64 s[10:11], s[12:13], s[10:11]
	s_or_b64 s[8:9], s[10:11], s[8:9]
	s_or_b64 s[6:7], s[8:9], s[6:7]
	s_or_b64 s[4:5], s[6:7], s[4:5]
	s_or_b64 s[2:3], s[4:5], s[2:3]
	s_or_b64 s[0:1], s[2:3], s[0:1]
	s_or_b64 vcc, s[0:1], vcc
	v_cndmask_b32_e64 v61, v68, v61, s[56:57]
	v_cndmask_b32_e64 v60, v68, v60, s[54:55]
	v_cndmask_b32_e64 v59, v68, v59, s[52:53]
	v_cndmask_b32_e64 v58, v68, v58, s[50:51]
	v_cndmask_b32_e64 v57, v68, v57, s[48:49]
	v_cndmask_b32_e64 v56, v68, v56, s[46:47]
	v_cndmask_b32_e64 v55, v68, v55, s[44:45]
	v_cndmask_b32_e64 v54, v68, v54, s[42:43]
	v_cndmask_b32_e64 v53, v68, v53, s[40:41]
	v_cndmask_b32_e64 v52, v68, v52, s[38:39]
	v_cndmask_b32_e64 v51, v68, v51, s[36:37]
	v_cndmask_b32_e64 v50, v68, v50, s[34:35]
	v_cndmask_b32_e64 v49, v68, v49, s[28:29]
	v_cndmask_b32_e64 v45, v68, v45, s[24:25]
	v_cndmask_b32_e64 v44, v68, v44, s[22:23]
	v_cndmask_b32_e64 v43, v68, v43, s[20:21]
	v_cndmask_b32_e64 v42, v68, v42, s[18:19]
	v_cndmask_b32_e64 v41, v68, v41, s[16:17]
	v_cndmask_b32_e64 v40, v68, v40, s[14:15]
	v_cndmask_b32_e64 v39, v68, v39, s[12:13]
	v_cndmask_b32_e64 v38, v68, v38, s[10:11]
	v_cndmask_b32_e64 v37, v68, v37, s[8:9]
	v_cndmask_b32_e64 v36, v68, v36, s[6:7]
	v_cndmask_b32_e64 v35, v68, v35, s[4:5]
	v_cndmask_b32_e64 v34, v68, v34, s[2:3]
	v_cndmask_b32_e64 v33, v68, v33, s[0:1]
	v_cndmask_b32_e32 v32, v68, v32, vcc

.LBB3_28:
	s_waitcnt lgkmcnt(14)
	v_mfma_f32_32x32x16_f16 v[0:15], v[156:159], v[192:195], v[0:15]
	v_exp_f32_e32 v48, v48
	v_exp_f32_e32 v49, v49
	v_exp_f32_e32 v50, v50
	v_exp_f32_e32 v51, v51
	s_waitcnt lgkmcnt(12)
	v_mfma_f32_32x32x16_f16 v[16:31], v[156:159], v[188:191], v[16:31]
	v_exp_f32_e32 v52, v52
	v_exp_f32_e32 v53, v53
	v_exp_f32_e32 v54, v54
	v_exp_f32_e32 v55, v55
	s_waitcnt lgkmcnt(10)
	v_mfma_f32_32x32x16_f16 v[0:15], v[152:155], v[124:127], v[0:15]
	v_exp_f32_e32 v56, v56
	v_exp_f32_e32 v57, v57
	v_exp_f32_e32 v58, v58
	v_exp_f32_e32 v59, v59
	s_waitcnt lgkmcnt(8)
	v_mfma_f32_32x32x16_f16 v[16:31], v[152:155], v[120:123], v[16:31]
	v_exp_f32_e32 v60, v60
	v_exp_f32_e32 v61, v61
	v_exp_f32_e32 v62, v62
	v_exp_f32_e32 v63, v63
	s_waitcnt lgkmcnt(6)
	v_mfma_f32_32x32x16_f16 v[0:15], v[148:151], v[116:119], v[0:15]
	v_exp_f32_e32 v32, v32
	v_exp_f32_e32 v33, v33
	v_exp_f32_e32 v34, v34
	v_exp_f32_e32 v35, v35
	s_waitcnt lgkmcnt(4)
	v_mfma_f32_32x32x16_f16 v[16:31], v[148:151], v[112:115], v[16:31]
	v_exp_f32_e32 v36, v36
	v_exp_f32_e32 v37, v37
	v_exp_f32_e32 v38, v38
	v_exp_f32_e32 v39, v39
	s_waitcnt lgkmcnt(2)
	v_mfma_f32_32x32x16_f16 v[0:15], v[144:147], v[82:85], v[0:15]
	v_exp_f32_e32 v40, v40
	v_exp_f32_e32 v41, v41
	v_exp_f32_e32 v42, v42
	v_exp_f32_e32 v43, v43
	s_waitcnt lgkmcnt(0)
	v_mfma_f32_32x32x16_f16 v[16:31], v[144:147], v[96:99], v[16:31]
	v_exp_f32_e32 v46, v46
	v_exp_f32_e32 v47, v47
	v_exp_f32_e32 v44, v44
	v_exp_f32_e32 v45, v45
	v_mov_b64_e32 v[94:95], v[46:47]
	v_mov_b64_e32 v[90:91], v[42:43]
	v_mov_b64_e32 v[92:93], v[44:45]
	v_mov_b64_e32 v[88:89], v[40:41]
	v_mov_b64_e32 v[86:87], v[38:39]
	v_mov_b64_e32 v[84:85], v[36:37]
	v_mov_b64_e32 v[82:83], v[34:35]
	v_mov_b64_e32 v[80:81], v[32:33]
	s_waitcnt vmcnt(2) lgkmcnt(0)
	s_barrier
	s_andn2_b64 vcc, exec, s[0:1]
	s_cbranch_vccnz .LBB3_30
	s_waitcnt lgkmcnt(0)
	v_lshl_add_u32 v44, v200, 4, s84
	ds_read_b128 v[32:35], v44 offset:49248
	ds_read_b128 v[36:39], v44 offset:49216
	ds_read_b128 v[40:43], v44 offset:49184
	ds_read_b128 v[44:47], v44 offset:49152
	s_waitcnt lgkmcnt(3)
	v_pk_mul_f32 v[14:15], v[14:15], v[34:35]
	s_waitcnt lgkmcnt(2)
	v_pk_mul_f32 v[10:11], v[10:11], v[38:39]
	s_waitcnt lgkmcnt(1)
	v_pk_mul_f32 v[6:7], v[6:7], v[42:43]
	s_waitcnt lgkmcnt(0)
	v_pk_mul_f32 v[2:3], v[2:3], v[46:47]
	v_pk_mul_f32 v[12:13], v[12:13], v[32:33]
	v_pk_mul_f32 v[8:9], v[8:9], v[36:37]
	v_pk_mul_f32 v[4:5], v[4:5], v[40:41]
	v_pk_mul_f32 v[0:1], v[0:1], v[44:45]
	v_pk_mul_f32 v[30:31], v[30:31], v[34:35]
	v_pk_mul_f32 v[26:27], v[26:27], v[38:39]
	v_pk_mul_f32 v[22:23], v[22:23], v[42:43]
	v_pk_mul_f32 v[18:19], v[18:19], v[46:47]
	v_pk_mul_f32 v[28:29], v[28:29], v[32:33]
	v_pk_mul_f32 v[24:25], v[24:25], v[36:37]
	v_pk_mul_f32 v[20:21], v[20:21], v[40:41]
	v_pk_mul_f32 v[16:17], v[16:17], v[44:45]

	.amdhsa_kernel _ZN12_GLOBAL__N_111attn_kernelEPKDF16_S1_S1_PKiPDF16_
		.amdhsa_group_segment_fixed_size 0
		.amdhsa_private_segment_fixed_size 0
		.amdhsa_kernarg_size 40
		.amdhsa_user_sgpr_count 2
		.amdhsa_user_sgpr_dispatch_ptr 0
		.amdhsa_user_sgpr_queue_ptr 0
		.amdhsa_user_sgpr_kernarg_segment_ptr 1
		.amdhsa_user_sgpr_dispatch_id 0
		.amdhsa_user_sgpr_kernarg_preload_length 0
		.amdhsa_user_sgpr_kernarg_preload_offset 0
		.amdhsa_user_sgpr_private_segment_size 0
		.amdhsa_uses_dynamic_stack 0
		.amdhsa_enable_private_segment 0
		.amdhsa_system_sgpr_workgroup_id_x 1
		.amdhsa_system_sgpr_workgroup_id_y 0
		.amdhsa_system_sgpr_workgroup_id_z 0
		.amdhsa_system_sgpr_workgroup_info 0
		.amdhsa_system_vgpr_workitem_id 0
		.amdhsa_next_free_vgpr 212
		.amdhsa_next_free_sgpr 102
		.amdhsa_accum_offset 212
		.amdhsa_reserve_vcc 1
		.amdhsa_float_round_mode_32 0
		.amdhsa_float_round_mode_16_64 0
		.amdhsa_float_denorm_mode_32 3
		.amdhsa_float_denorm_mode_16_64 3
		.amdhsa_dx10_clamp 1
		.amdhsa_ieee_mode 1
		.amdhsa_fp16_overflow 0
		.amdhsa_tg_split 0
		.amdhsa_exception_fp_ieee_invalid_op 0
		.amdhsa_exception_fp_denorm_src 0
		.amdhsa_exception_fp_ieee_div_zero 0
		.amdhsa_exception_fp_ieee_overflow 0
		.amdhsa_exception_fp_ieee_underflow 0
		.amdhsa_exception_fp_ieee_inexact 0
		.amdhsa_exception_int_div_zero 0
	.end_amdhsa_kernel
